# first-layer out-projection epilogue: f32 residual loads of groups 0..8 issued together at the head and later groups 2-7 groups ahead (spare + bf16-path staging quads), counted waits
# baseline (speedup 1.0000x reference)
;     __device__ __forceinline__ void operator()(const Acc& acc, const Unit& u, int wr, int wc, int fr, int fq, const LAS float* tab) const {
;     ...
;                 const size_t row = (size_t)u.pm * BM + ai * HALF + wr * 64 + m * 16 + fr; const size_t off = row * D + col0; float ss = 0.f;
; #pragma unroll
;                 for (int bj = 0; bj < 2; ++bj) { f32x4 b0, b1;
;                     if (base32) { b0 = __builtin_nontemporal_load((const f32x4*)(base32 + off + bj * HALF)); b1 = __builtin_nontemporal_load((const f32x4*)(base32 + off + bj * HALF + 4)); }
;                     else { const u32x4 b4 = rb[ai][m][bj];
;                         b0 = (f32x4){__uint_as_float(b4.x << 16), __uint_as_float(b4.x & 0xFFFF0000u), __uint_as_float(b4.y << 16), __uint_as_float(b4.y & 0xFFFF0000u)};
;                         b1 = (f32x4){__uint_as_float(b4.z << 16), __uint_as_float(b4.z & 0xFFFF0000u), __uint_as_float(b4.w << 16), __uint_as_float(b4.w & 0xFFFF0000u)}; }
;                     const f32x4 o0 = b0 + acc[ai][bj][m][0], o1 = b1 + acc[ai][bj][m][1];
.LBB0_1864:
	v_lshlrev_b64 v[194:195], 10, v[220:221]
	v_lshl_add_u64 v[224:225], v[194:195], 0, v[218:219]
	v_cndmask_b32_e64 v194, 0, 1, s[18:19]
	s_mov_b64 s[34:35], -1
	v_cmp_ne_u32_e64 s[8:9], 1, v194
	s_andn2_b64 vcc, exec, s[18:19]
	v_lshl_add_u64 v[222:223], v[224:225], 2, s[10:11]
	s_cbranch_vccnz .LBB0_1866
	global_load_dwordx4 v[198:201], v[222:223], off offset:16 nt
	global_load_dwordx4 v[194:197], v[222:223], off nt
	v_mov_b64_e32 v[252:253], v[222:223]
	s_mov_b64 s[100:101], 0x200
	v_lshl_add_u64 v[226:227], v[222:223], 0, s[100:101]
	global_load_dwordx4 v[244:247], v[226:227], off offset:16 nt
	global_load_dwordx4 v[248:251], v[226:227], off nt
	s_mov_b64 s[100:101], 0x10000
	v_lshl_add_u64 v[226:227], v[222:223], 0, s[100:101]
	global_load_dwordx4 v[182:185], v[226:227], off offset:16 nt
	global_load_dwordx4 v[178:181], v[226:227], off nt
	s_mov_b64 s[100:101], 0x10200
	v_lshl_add_u64 v[226:227], v[222:223], 0, s[100:101]
	global_load_dwordx4 v[174:177], v[226:227], off offset:16 nt
	global_load_dwordx4 v[170:173], v[226:227], off nt
	s_mov_b64 s[100:101], 0x20000
	v_lshl_add_u64 v[226:227], v[222:223], 0, s[100:101]
	global_load_dwordx4 v[166:169], v[226:227], off offset:16 nt
	global_load_dwordx4 v[154:157], v[226:227], off nt
	s_mov_b64 s[100:101], 0x20200
	v_lshl_add_u64 v[226:227], v[222:223], 0, s[100:101]
	global_load_dwordx4 v[142:145], v[226:227], off offset:16 nt
	global_load_dwordx4 v[138:141], v[226:227], off nt
	s_mov_b64 s[100:101], 0x30000
	v_lshl_add_u64 v[226:227], v[222:223], 0, s[100:101]
	global_load_dwordx4 v[122:125], v[226:227], off offset:16 nt
	global_load_dwordx4 v[114:117], v[226:227], off nt
	s_mov_b64 s[100:101], 0x30200
	v_lshl_add_u64 v[226:227], v[222:223], 0, s[100:101]
	global_load_dwordx4 v[102:105], v[226:227], off offset:16 nt
	global_load_dwordx4 v[90:93], v[226:227], off nt
	s_mov_b64 s[100:101], 0x80000
	v_lshl_add_u64 v[226:227], v[222:223], 0, s[100:101]
	global_load_dwordx4 v[78:81], v[226:227], off offset:16 nt
	global_load_dwordx4 v[66:69], v[226:227], off nt
	s_waitcnt vmcnt(16)
	s_mov_b64 s[34:35], 0

; __device__ __forceinline__ void st16_wt(void* p, u32x4 v) { asm volatile("global_store_dwordx4 %0, %1, off sc1\n\ts_nop 1" :: "v"(p), "v"(v) : "memory"); }
; __device__ __forceinline__ unsigned cvt_pk_bf16(float lo, float hi) { unsigned r; asm volatile("v_cvt_pk_bf16_f32 %0, %1, %2" : "=v"(r) : "v"(lo), "v"(hi)); return r; }
;     __device__ __forceinline__ void operator()(const Acc& acc, const Unit& u, int wr, int wc, int fr, int fq, const LAS float* tab) const {
;     ...
;                 for (int bj = 0; bj < 2; ++bj) { f32x4 b0, b1;
;                     if (base32) { b0 = __builtin_nontemporal_load((const f32x4*)(base32 + off + bj * HALF)); b1 = __builtin_nontemporal_load((const f32x4*)(base32 + off + bj * HALF + 4)); }
;                     else { const u32x4 b4 = rb[ai][m][bj];
;                         b0 = (f32x4){__uint_as_float(b4.x << 16), __uint_as_float(b4.x & 0xFFFF0000u), __uint_as_float(b4.y << 16), __uint_as_float(b4.y & 0xFFFF0000u)};
;                         b1 = (f32x4){__uint_as_float(b4.z << 16), __uint_as_float(b4.z & 0xFFFF0000u), __uint_as_float(b4.w << 16), __uint_as_float(b4.w & 0xFFFF0000u)}; }
;                     const f32x4 o0 = b0 + acc[ai][bj][m][0], o1 = b1 + acc[ai][bj][m][1];
;                     if (out32) {
;                         if (!dry) { *(f32x4*)(out32 + off + bj * HALF) = o0; *(f32x4*)(out32 + off + bj * HALF + 4) = o1; }
;                         continue; }
;                     ss += ((o0[0] * o0[0] + o0[1] * o0[1]) + (o0[2] * o0[2] + o0[3] * o0[3])) + ((o1[0] * o1[0] + o1[1] * o1[1]) + (o1[2] * o1[2] + o1[3] * o1[3]));
;                     u32x4 w; w.x = cvt_pk_bf16(o0[0], o0[1]); w.y = cvt_pk_bf16(o0[2], o0[3]); w.z = cvt_pk_bf16(o1[0], o1[1]); w.w = cvt_pk_bf16(o1[2], o1[3]);
;                     if (!dry) st16_wt(xb + off + bj * HALF, w); }
.LBB0_1868:
	v_lshl_add_u64 v[190:191], v[224:225], 1, s[14:15]
	v_pk_add_f32 v[192:193], v[164:165], v[196:197]
	v_pk_add_f32 v[196:197], v[162:163], v[194:195]
	v_pk_add_f32 v[194:195], v[160:161], v[200:201]
	v_pk_add_f32 v[198:199], v[158:159], v[198:199]
	v_cvt_pk_bf16_f32 v158, v196, v197
	v_cvt_pk_bf16_f32 v159, v192, v193
	s_and_b64 vcc, exec, s[8:9]
	v_cvt_pk_bf16_f32 v160, v198, v199
	v_cvt_pk_bf16_f32 v161, v194, v195
	s_mov_b64 s[34:35], -1
	global_store_dwordx4 v[190:191], v[158:161], off sc1
	s_nop 1
	s_cbranch_vccnz .LBB0_1870
	s_waitcnt vmcnt(14)
	s_nop 1
	v_mov_b32_e32 v162, v244
	v_mov_b32_e32 v163, v245
	v_mov_b32_e32 v164, v246
	v_mov_b32_e32 v165, v247
	v_mov_b32_e32 v158, v248
	v_mov_b32_e32 v159, v249
	v_mov_b32_e32 v160, v250
	v_mov_b32_e32 v161, v251
	s_mov_b64 s[34:35], 0

;     __device__ __forceinline__ void operator()(const Acc& acc, const Unit& u, int wr, int wc, int fr, int fq, const LAS float* tab) const {
;     ...
;                 const size_t row = (size_t)u.pm * BM + ai * HALF + wr * 64 + m * 16 + fr; const size_t off = row * D + col0; float ss = 0.f;
; #pragma unroll
;                 for (int bj = 0; bj < 2; ++bj) { f32x4 b0, b1;
;                     if (base32) { b0 = __builtin_nontemporal_load((const f32x4*)(base32 + off + bj * HALF)); b1 = __builtin_nontemporal_load((const f32x4*)(base32 + off + bj * HALF + 4)); }
.LBB0_1874:
	s_or_b64 exec, exec, s[34:35]
	v_or_b32_e32 v158, 16, v220
	v_mov_b32_e32 v159, v221
	v_lshlrev_b64 v[146:147], 10, v[158:159]
	v_lshl_add_u64 v[160:161], v[146:147], 0, v[218:219]
	s_mov_b64 s[34:35], -1
	s_and_b64 vcc, exec, s[8:9]
	v_lshl_add_u64 v[162:163], v[160:161], 2, s[10:11]
	s_cbranch_vccnz .LBB0_1876
	s_mov_b64 s[100:101], 0x80200
	v_lshl_add_u64 v[226:227], v[252:253], 0, s[100:101]
	global_load_dwordx4 v[244:247], v[226:227], off offset:16 nt
	global_load_dwordx4 v[248:251], v[226:227], off nt
	s_waitcnt vmcnt(14)
	s_nop 1
	v_mov_b32_e32 v150, v182
	v_mov_b32_e32 v151, v183
	v_mov_b32_e32 v152, v184
	v_mov_b32_e32 v153, v185
	v_mov_b32_e32 v146, v178
	v_mov_b32_e32 v147, v179
	v_mov_b32_e32 v148, v180
	v_mov_b32_e32 v149, v181
	s_mov_b64 s[34:35], 0

; __device__ __forceinline__ void st16_wt(void* p, u32x4 v) { asm volatile("global_store_dwordx4 %0, %1, off sc1\n\ts_nop 1" :: "v"(p), "v"(v) : "memory"); }
; __device__ __forceinline__ unsigned cvt_pk_bf16(float lo, float hi) { unsigned r; asm volatile("v_cvt_pk_bf16_f32 %0, %1, %2" : "=v"(r) : "v"(lo), "v"(hi)); return r; }
;     __device__ __forceinline__ void operator()(const Acc& acc, const Unit& u, int wr, int wc, int fr, int fq, const LAS float* tab) const {
;     ...
;                 for (int bj = 0; bj < 2; ++bj) { f32x4 b0, b1;
;                     if (base32) { b0 = __builtin_nontemporal_load((const f32x4*)(base32 + off + bj * HALF)); b1 = __builtin_nontemporal_load((const f32x4*)(base32 + off + bj * HALF + 4)); }
;                     else { const u32x4 b4 = rb[ai][m][bj];
;                         b0 = (f32x4){__uint_as_float(b4.x << 16), __uint_as_float(b4.x & 0xFFFF0000u), __uint_as_float(b4.y << 16), __uint_as_float(b4.y & 0xFFFF0000u)};
;                         b1 = (f32x4){__uint_as_float(b4.z << 16), __uint_as_float(b4.z & 0xFFFF0000u), __uint_as_float(b4.w << 16), __uint_as_float(b4.w & 0xFFFF0000u)}; }
;                     const f32x4 o0 = b0 + acc[ai][bj][m][0], o1 = b1 + acc[ai][bj][m][1];
;                     if (out32) {
;                         if (!dry) { *(f32x4*)(out32 + off + bj * HALF) = o0; *(f32x4*)(out32 + off + bj * HALF + 4) = o1; }
;                         continue; }
;                     ss += ((o0[0] * o0[0] + o0[1] * o0[1]) + (o0[2] * o0[2] + o0[3] * o0[3])) + ((o1[0] * o1[0] + o1[1] * o1[1]) + (o1[2] * o1[2] + o1[3] * o1[3]));
;                     u32x4 w; w.x = cvt_pk_bf16(o0[0], o0[1]); w.y = cvt_pk_bf16(o0[2], o0[3]); w.z = cvt_pk_bf16(o1[0], o1[1]); w.w = cvt_pk_bf16(o1[2], o1[3]);
;                     if (!dry) st16_wt(xb + off + bj * HALF, w); }
.LBB0_1878:
	v_lshl_add_u64 v[160:161], v[160:161], 1, s[14:15]
	v_pk_add_f32 v[148:149], v[136:137], v[148:149]
	v_pk_add_f32 v[164:165], v[134:135], v[146:147]
	v_pk_add_f32 v[146:147], v[132:133], v[152:153]
	v_pk_add_f32 v[150:151], v[130:131], v[150:151]
	v_cvt_pk_bf16_f32 v130, v164, v165
	v_cvt_pk_bf16_f32 v131, v148, v149
	s_and_b64 vcc, exec, s[8:9]
	v_cvt_pk_bf16_f32 v132, v150, v151
	v_cvt_pk_bf16_f32 v133, v146, v147
	s_mov_b64 s[34:35], -1
	global_store_dwordx4 v[160:161], v[130:133], off sc1
	s_nop 1
	s_cbranch_vccnz .LBB0_1880
	s_waitcnt vmcnt(12)
	s_nop 1
	v_mov_b32_e32 v134, v174
	v_mov_b32_e32 v135, v175
	v_mov_b32_e32 v136, v176
	v_mov_b32_e32 v137, v177
	v_mov_b32_e32 v130, v170
	v_mov_b32_e32 v131, v171
	v_mov_b32_e32 v132, v172
	v_mov_b32_e32 v133, v173
	s_mov_b64 s[34:35], 0

;     __device__ __forceinline__ void operator()(const Acc& acc, const Unit& u, int wr, int wc, int fr, int fq, const LAS float* tab) const {
;     ...
;                 const size_t row = (size_t)u.pm * BM + ai * HALF + wr * 64 + m * 16 + fr; const size_t off = row * D + col0; float ss = 0.f;
; #pragma unroll
;                 for (int bj = 0; bj < 2; ++bj) { f32x4 b0, b1;
;                     if (base32) { b0 = __builtin_nontemporal_load((const f32x4*)(base32 + off + bj * HALF)); b1 = __builtin_nontemporal_load((const f32x4*)(base32 + off + bj * HALF + 4)); }
.LBB0_1884:
	s_or_b64 exec, exec, s[34:35]
	v_or_b32_e32 v130, 32, v220
	v_mov_b32_e32 v131, v221
	v_lshlrev_b64 v[118:119], 10, v[130:131]
	v_lshl_add_u64 v[132:133], v[118:119], 0, v[218:219]
	s_mov_b64 s[34:35], -1
	s_and_b64 vcc, exec, s[8:9]
	v_lshl_add_u64 v[134:135], v[132:133], 2, s[10:11]
	s_cbranch_vccnz .LBB0_1886
	s_waitcnt vmcnt(10)
	s_nop 1
	v_mov_b32_e32 v126, v166
	v_mov_b32_e32 v127, v167
	v_mov_b32_e32 v128, v168
	v_mov_b32_e32 v129, v169
	v_mov_b32_e32 v118, v154
	v_mov_b32_e32 v119, v155
	v_mov_b32_e32 v120, v156
	v_mov_b32_e32 v121, v157
	s_mov_b64 s[34:35], 0

; __device__ __forceinline__ void st16_wt(void* p, u32x4 v) { asm volatile("global_store_dwordx4 %0, %1, off sc1\n\ts_nop 1" :: "v"(p), "v"(v) : "memory"); }
; __device__ __forceinline__ unsigned cvt_pk_bf16(float lo, float hi) { unsigned r; asm volatile("v_cvt_pk_bf16_f32 %0, %1, %2" : "=v"(r) : "v"(lo), "v"(hi)); return r; }
;     __device__ __forceinline__ void operator()(const Acc& acc, const Unit& u, int wr, int wc, int fr, int fq, const LAS float* tab) const {
;     ...
;                 for (int bj = 0; bj < 2; ++bj) { f32x4 b0, b1;
;                     if (base32) { b0 = __builtin_nontemporal_load((const f32x4*)(base32 + off + bj * HALF)); b1 = __builtin_nontemporal_load((const f32x4*)(base32 + off + bj * HALF + 4)); }
;                     else { const u32x4 b4 = rb[ai][m][bj];
;                         b0 = (f32x4){__uint_as_float(b4.x << 16), __uint_as_float(b4.x & 0xFFFF0000u), __uint_as_float(b4.y << 16), __uint_as_float(b4.y & 0xFFFF0000u)};
;                         b1 = (f32x4){__uint_as_float(b4.z << 16), __uint_as_float(b4.z & 0xFFFF0000u), __uint_as_float(b4.w << 16), __uint_as_float(b4.w & 0xFFFF0000u)}; }
;                     const f32x4 o0 = b0 + acc[ai][bj][m][0], o1 = b1 + acc[ai][bj][m][1];
;                     if (out32) {
;                         if (!dry) { *(f32x4*)(out32 + off + bj * HALF) = o0; *(f32x4*)(out32 + off + bj * HALF + 4) = o1; }
;                         continue; }
;                     ss += ((o0[0] * o0[0] + o0[1] * o0[1]) + (o0[2] * o0[2] + o0[3] * o0[3])) + ((o1[0] * o1[0] + o1[1] * o1[1]) + (o1[2] * o1[2] + o1[3] * o1[3]));
;                     u32x4 w; w.x = cvt_pk_bf16(o0[0], o0[1]); w.y = cvt_pk_bf16(o0[2], o0[3]); w.z = cvt_pk_bf16(o1[0], o1[1]); w.w = cvt_pk_bf16(o1[2], o1[3]);
;                     if (!dry) st16_wt(xb + off + bj * HALF, w); }
.LBB0_1888:
	v_lshl_add_u64 v[132:133], v[132:133], 1, s[14:15]
	v_pk_add_f32 v[120:121], v[112:113], v[120:121]
	v_pk_add_f32 v[136:137], v[110:111], v[118:119]
	v_pk_add_f32 v[118:119], v[108:109], v[128:129]
	v_pk_add_f32 v[126:127], v[106:107], v[126:127]
	v_cvt_pk_bf16_f32 v106, v136, v137
	v_cvt_pk_bf16_f32 v107, v120, v121
	s_and_b64 vcc, exec, s[8:9]
	v_cvt_pk_bf16_f32 v108, v126, v127
	v_cvt_pk_bf16_f32 v109, v118, v119
	s_mov_b64 s[34:35], -1
	global_store_dwordx4 v[132:133], v[106:109], off sc1
	s_nop 1
	s_cbranch_vccnz .LBB0_1890
	s_waitcnt vmcnt(8)
	s_nop 1
	v_mov_b32_e32 v110, v142
	v_mov_b32_e32 v111, v143
	v_mov_b32_e32 v112, v144
	v_mov_b32_e32 v113, v145
	v_mov_b32_e32 v106, v138
	v_mov_b32_e32 v107, v139
	v_mov_b32_e32 v108, v140
	v_mov_b32_e32 v109, v141
	s_mov_b64 s[34:35], 0

;     __device__ __forceinline__ void operator()(const Acc& acc, const Unit& u, int wr, int wc, int fr, int fq, const LAS float* tab) const {
;     ...
;                 const size_t row = (size_t)u.pm * BM + ai * HALF + wr * 64 + m * 16 + fr; const size_t off = row * D + col0; float ss = 0.f;
; #pragma unroll
;                 for (int bj = 0; bj < 2; ++bj) { f32x4 b0, b1;
;                     if (base32) { b0 = __builtin_nontemporal_load((const f32x4*)(base32 + off + bj * HALF)); b1 = __builtin_nontemporal_load((const f32x4*)(base32 + off + bj * HALF + 4)); }
.LBB0_1894:
	s_or_b64 exec, exec, s[34:35]
	v_or_b32_e32 v106, 48, v220
	v_mov_b32_e32 v107, v221
	v_lshlrev_b64 v[94:95], 10, v[106:107]
	v_lshl_add_u64 v[108:109], v[94:95], 0, v[218:219]
	s_mov_b64 s[34:35], -1
	s_and_b64 vcc, exec, s[8:9]
	v_lshl_add_u64 v[110:111], v[108:109], 2, s[10:11]
	s_cbranch_vccnz .LBB0_1896
	s_waitcnt vmcnt(6)
	s_nop 1
	v_mov_b32_e32 v98, v122
	v_mov_b32_e32 v99, v123
	v_mov_b32_e32 v100, v124
	v_mov_b32_e32 v101, v125
	v_mov_b32_e32 v94, v114
	v_mov_b32_e32 v95, v115
	v_mov_b32_e32 v96, v116
	v_mov_b32_e32 v97, v117
	s_mov_b64 s[100:101], 0x90000
	v_lshl_add_u64 v[226:227], v[252:253], 0, s[100:101]
	global_load_dwordx4 v[122:125], v[226:227], off offset:16 nt
	global_load_dwordx4 v[114:117], v[226:227], off nt
	s_mov_b64 s[34:35], 0

; __device__ __forceinline__ void st16_wt(void* p, u32x4 v) { asm volatile("global_store_dwordx4 %0, %1, off sc1\n\ts_nop 1" :: "v"(p), "v"(v) : "memory"); }
; __device__ __forceinline__ unsigned cvt_pk_bf16(float lo, float hi) { unsigned r; asm volatile("v_cvt_pk_bf16_f32 %0, %1, %2" : "=v"(r) : "v"(lo), "v"(hi)); return r; }
;     __device__ __forceinline__ void operator()(const Acc& acc, const Unit& u, int wr, int wc, int fr, int fq, const LAS float* tab) const {
;     ...
;                 for (int bj = 0; bj < 2; ++bj) { f32x4 b0, b1;
;                     if (base32) { b0 = __builtin_nontemporal_load((const f32x4*)(base32 + off + bj * HALF)); b1 = __builtin_nontemporal_load((const f32x4*)(base32 + off + bj * HALF + 4)); }
;                     else { const u32x4 b4 = rb[ai][m][bj];
;                         b0 = (f32x4){__uint_as_float(b4.x << 16), __uint_as_float(b4.x & 0xFFFF0000u), __uint_as_float(b4.y << 16), __uint_as_float(b4.y & 0xFFFF0000u)};
;                         b1 = (f32x4){__uint_as_float(b4.z << 16), __uint_as_float(b4.z & 0xFFFF0000u), __uint_as_float(b4.w << 16), __uint_as_float(b4.w & 0xFFFF0000u)}; }
;                     const f32x4 o0 = b0 + acc[ai][bj][m][0], o1 = b1 + acc[ai][bj][m][1];
;                     if (out32) {
;                         if (!dry) { *(f32x4*)(out32 + off + bj * HALF) = o0; *(f32x4*)(out32 + off + bj * HALF + 4) = o1; }
;                         continue; }
;                     ss += ((o0[0] * o0[0] + o0[1] * o0[1]) + (o0[2] * o0[2] + o0[3] * o0[3])) + ((o1[0] * o1[0] + o1[1] * o1[1]) + (o1[2] * o1[2] + o1[3] * o1[3]));
;                     u32x4 w; w.x = cvt_pk_bf16(o0[0], o0[1]); w.y = cvt_pk_bf16(o0[2], o0[3]); w.z = cvt_pk_bf16(o1[0], o1[1]); w.w = cvt_pk_bf16(o1[2], o1[3]);
;                     if (!dry) st16_wt(xb + off + bj * HALF, w); }
.LBB0_1898:
	v_lshl_add_u64 v[108:109], v[108:109], 1, s[14:15]
	v_pk_add_f32 v[96:97], v[88:89], v[96:97]
	v_pk_add_f32 v[112:113], v[86:87], v[94:95]
	v_pk_add_f32 v[94:95], v[84:85], v[100:101]
	v_pk_add_f32 v[98:99], v[82:83], v[98:99]
	v_cvt_pk_bf16_f32 v82, v112, v113
	v_cvt_pk_bf16_f32 v83, v96, v97
	s_and_b64 vcc, exec, s[8:9]
	v_cvt_pk_bf16_f32 v84, v98, v99
	v_cvt_pk_bf16_f32 v85, v94, v95
	s_mov_b64 s[34:35], -1
	global_store_dwordx4 v[108:109], v[82:85], off sc1
	s_nop 1
	s_cbranch_vccnz .LBB0_1900
	s_waitcnt vmcnt(6)
	s_nop 1
	v_mov_b32_e32 v86, v102
	v_mov_b32_e32 v87, v103
	v_mov_b32_e32 v88, v104
	v_mov_b32_e32 v89, v105
	v_mov_b32_e32 v82, v90
	v_mov_b32_e32 v83, v91
	v_mov_b32_e32 v84, v92
	v_mov_b32_e32 v85, v93
	s_mov_b64 s[100:101], 0x90200
	v_lshl_add_u64 v[226:227], v[252:253], 0, s[100:101]
	global_load_dwordx4 v[102:105], v[226:227], off offset:16 nt
	global_load_dwordx4 v[90:93], v[226:227], off nt
	s_mov_b64 s[34:35], 0

;     __device__ __forceinline__ void operator()(const Acc& acc, const Unit& u, int wr, int wc, int fr, int fq, const LAS float* tab) const {
;     ...
;                 const size_t row = (size_t)u.pm * BM + ai * HALF + wr * 64 + m * 16 + fr; const size_t off = row * D + col0; float ss = 0.f;
; #pragma unroll
;                 for (int bj = 0; bj < 2; ++bj) { f32x4 b0, b1;
;                     if (base32) { b0 = __builtin_nontemporal_load((const f32x4*)(base32 + off + bj * HALF)); b1 = __builtin_nontemporal_load((const f32x4*)(base32 + off + bj * HALF + 4)); }
.LBB0_1904:
	s_or_b64 exec, exec, s[34:35]
	v_lshl_add_u64 v[82:83], v[220:221], 0, s[90:91]
	v_lshlrev_b64 v[70:71], 10, v[82:83]
	v_lshl_add_u64 v[84:85], v[70:71], 0, v[218:219]
	s_mov_b64 s[34:35], -1
	s_and_b64 vcc, exec, s[8:9]
	v_lshl_add_u64 v[86:87], v[84:85], 2, s[10:11]
	s_cbranch_vccnz .LBB0_1906
	s_waitcnt vmcnt(6)
	s_nop 1
	v_mov_b32_e32 v74, v78
	v_mov_b32_e32 v75, v79
	v_mov_b32_e32 v76, v80
	v_mov_b32_e32 v77, v81
	v_mov_b32_e32 v70, v66
	v_mov_b32_e32 v71, v67
	v_mov_b32_e32 v72, v68
	v_mov_b32_e32 v73, v69
	s_mov_b64 s[100:101], 0xa0000
	v_lshl_add_u64 v[226:227], v[252:253], 0, s[100:101]
	global_load_dwordx4 v[78:81], v[226:227], off offset:16 nt
	global_load_dwordx4 v[66:69], v[226:227], off nt
	s_mov_b64 s[34:35], 0

; __device__ __forceinline__ void st16_wt(void* p, u32x4 v) { asm volatile("global_store_dwordx4 %0, %1, off sc1\n\ts_nop 1" :: "v"(p), "v"(v) : "memory"); }
; __device__ __forceinline__ unsigned cvt_pk_bf16(float lo, float hi) { unsigned r; asm volatile("v_cvt_pk_bf16_f32 %0, %1, %2" : "=v"(r) : "v"(lo), "v"(hi)); return r; }
;     __device__ __forceinline__ void operator()(const Acc& acc, const Unit& u, int wr, int wc, int fr, int fq, const LAS float* tab) const {
;     ...
;                 for (int bj = 0; bj < 2; ++bj) { f32x4 b0, b1;
;                     if (base32) { b0 = __builtin_nontemporal_load((const f32x4*)(base32 + off + bj * HALF)); b1 = __builtin_nontemporal_load((const f32x4*)(base32 + off + bj * HALF + 4)); }
;                     else { const u32x4 b4 = rb[ai][m][bj];
;                         b0 = (f32x4){__uint_as_float(b4.x << 16), __uint_as_float(b4.x & 0xFFFF0000u), __uint_as_float(b4.y << 16), __uint_as_float(b4.y & 0xFFFF0000u)};
;                         b1 = (f32x4){__uint_as_float(b4.z << 16), __uint_as_float(b4.z & 0xFFFF0000u), __uint_as_float(b4.w << 16), __uint_as_float(b4.w & 0xFFFF0000u)}; }
;                     const f32x4 o0 = b0 + acc[ai][bj][m][0], o1 = b1 + acc[ai][bj][m][1];
;                     if (out32) {
;                         if (!dry) { *(f32x4*)(out32 + off + bj * HALF) = o0; *(f32x4*)(out32 + off + bj * HALF + 4) = o1; }
;                         continue; }
;                     ss += ((o0[0] * o0[0] + o0[1] * o0[1]) + (o0[2] * o0[2] + o0[3] * o0[3])) + ((o1[0] * o1[0] + o1[1] * o1[1]) + (o1[2] * o1[2] + o1[3] * o1[3]));
;                     u32x4 w; w.x = cvt_pk_bf16(o0[0], o0[1]); w.y = cvt_pk_bf16(o0[2], o0[3]); w.z = cvt_pk_bf16(o1[0], o1[1]); w.w = cvt_pk_bf16(o1[2], o1[3]);
;                     if (!dry) st16_wt(xb + off + bj * HALF, w); }
.LBB0_1908:
	v_lshl_add_u64 v[84:85], v[84:85], 1, s[14:15]
	v_pk_add_f32 v[72:73], v[64:65], v[72:73]
	v_pk_add_f32 v[88:89], v[62:63], v[70:71]
	v_pk_add_f32 v[70:71], v[60:61], v[76:77]
	v_pk_add_f32 v[74:75], v[58:59], v[74:75]
	v_cvt_pk_bf16_f32 v58, v88, v89
	v_cvt_pk_bf16_f32 v59, v72, v73
	s_and_b64 vcc, exec, s[8:9]
	v_cvt_pk_bf16_f32 v60, v74, v75
	v_cvt_pk_bf16_f32 v61, v70, v71
	s_mov_b64 s[34:35], -1
	global_store_dwordx4 v[84:85], v[58:61], off sc1
	s_nop 1
	s_cbranch_vccnz .LBB0_1910
	s_waitcnt vmcnt(6)
	s_nop 1
	v_mov_b32_e32 v62, v244
	v_mov_b32_e32 v63, v245
	v_mov_b32_e32 v64, v246
	v_mov_b32_e32 v65, v247
	v_mov_b32_e32 v58, v248
	v_mov_b32_e32 v59, v249
	v_mov_b32_e32 v60, v250
	v_mov_b32_e32 v61, v251
	s_mov_b64 s[100:101], 0xa0200
	v_lshl_add_u64 v[226:227], v[252:253], 0, s[100:101]
	global_load_dwordx4 v[244:247], v[226:227], off offset:16 nt
	global_load_dwordx4 v[248:251], v[226:227], off nt
	s_mov_b64 s[34:35], 0

;     __device__ __forceinline__ void operator()(const Acc& acc, const Unit& u, int wr, int wc, int fr, int fq, const LAS float* tab) const {
;     ...
;                 const size_t row = (size_t)u.pm * BM + ai * HALF + wr * 64 + m * 16 + fr; const size_t off = row * D + col0; float ss = 0.f;
; #pragma unroll
;                 for (int bj = 0; bj < 2; ++bj) { f32x4 b0, b1;
;                     if (base32) { b0 = __builtin_nontemporal_load((const f32x4*)(base32 + off + bj * HALF)); b1 = __builtin_nontemporal_load((const f32x4*)(base32 + off + bj * HALF + 4)); }
.LBB0_1914:
	s_or_b64 exec, exec, s[34:35]
	s_mov_b64 s[0:1], 0x90
	v_lshl_add_u64 v[58:59], v[220:221], 0, s[0:1]
	v_lshlrev_b64 v[50:51], 10, v[58:59]
	v_lshl_add_u64 v[60:61], v[50:51], 0, v[218:219]
	s_mov_b64 s[34:35], -1
	s_and_b64 vcc, exec, s[8:9]
	v_lshl_add_u64 v[62:63], v[60:61], 2, s[10:11]
	s_cbranch_vccnz .LBB0_1916
	s_waitcnt vmcnt(6)
	s_nop 1
	v_mov_b32_e32 v54, v122
	v_mov_b32_e32 v55, v123
	v_mov_b32_e32 v56, v124
	v_mov_b32_e32 v57, v125
	v_mov_b32_e32 v50, v114
	v_mov_b32_e32 v51, v115
	v_mov_b32_e32 v52, v116
	v_mov_b32_e32 v53, v117
	s_mov_b64 s[34:35], 0

; __device__ __forceinline__ void st16_wt(void* p, u32x4 v) { asm volatile("global_store_dwordx4 %0, %1, off sc1\n\ts_nop 1" :: "v"(p), "v"(v) : "memory"); }
; __device__ __forceinline__ unsigned cvt_pk_bf16(float lo, float hi) { unsigned r; asm volatile("v_cvt_pk_bf16_f32 %0, %1, %2" : "=v"(r) : "v"(lo), "v"(hi)); return r; }
;     __device__ __forceinline__ void operator()(const Acc& acc, const Unit& u, int wr, int wc, int fr, int fq, const LAS float* tab) const {
;     ...
;                 for (int bj = 0; bj < 2; ++bj) { f32x4 b0, b1;
;                     if (base32) { b0 = __builtin_nontemporal_load((const f32x4*)(base32 + off + bj * HALF)); b1 = __builtin_nontemporal_load((const f32x4*)(base32 + off + bj * HALF + 4)); }
;                     else { const u32x4 b4 = rb[ai][m][bj];
;                         b0 = (f32x4){__uint_as_float(b4.x << 16), __uint_as_float(b4.x & 0xFFFF0000u), __uint_as_float(b4.y << 16), __uint_as_float(b4.y & 0xFFFF0000u)};
;                         b1 = (f32x4){__uint_as_float(b4.z << 16), __uint_as_float(b4.z & 0xFFFF0000u), __uint_as_float(b4.w << 16), __uint_as_float(b4.w & 0xFFFF0000u)}; }
;                     const f32x4 o0 = b0 + acc[ai][bj][m][0], o1 = b1 + acc[ai][bj][m][1];
;                     if (out32) {
;                         if (!dry) { *(f32x4*)(out32 + off + bj * HALF) = o0; *(f32x4*)(out32 + off + bj * HALF + 4) = o1; }
;                         continue; }
;                     ss += ((o0[0] * o0[0] + o0[1] * o0[1]) + (o0[2] * o0[2] + o0[3] * o0[3])) + ((o1[0] * o1[0] + o1[1] * o1[1]) + (o1[2] * o1[2] + o1[3] * o1[3]));
;                     u32x4 w; w.x = cvt_pk_bf16(o0[0], o0[1]); w.y = cvt_pk_bf16(o0[2], o0[3]); w.z = cvt_pk_bf16(o1[0], o1[1]); w.w = cvt_pk_bf16(o1[2], o1[3]);
;                     if (!dry) st16_wt(xb + off + bj * HALF, w); }
.LBB0_1918:
	v_lshl_add_u64 v[60:61], v[60:61], 1, s[14:15]
	v_pk_add_f32 v[52:53], v[48:49], v[52:53]
	v_pk_add_f32 v[64:65], v[46:47], v[50:51]
	v_pk_add_f32 v[50:51], v[44:45], v[56:57]
	v_pk_add_f32 v[54:55], v[42:43], v[54:55]
	v_cvt_pk_bf16_f32 v42, v64, v65
	v_cvt_pk_bf16_f32 v43, v52, v53
	s_and_b64 vcc, exec, s[8:9]
	v_cvt_pk_bf16_f32 v44, v54, v55
	v_cvt_pk_bf16_f32 v45, v50, v51
	s_mov_b64 s[34:35], -1
	global_store_dwordx4 v[60:61], v[42:45], off sc1
	s_nop 1
	s_cbranch_vccnz .LBB0_1920
	s_waitcnt vmcnt(4)
	s_nop 1
	v_mov_b32_e32 v46, v102
	v_mov_b32_e32 v47, v103
	v_mov_b32_e32 v48, v104
	v_mov_b32_e32 v49, v105
	v_mov_b32_e32 v42, v90
	v_mov_b32_e32 v43, v91
	v_mov_b32_e32 v44, v92
	v_mov_b32_e32 v45, v93
	s_mov_b64 s[34:35], 0

;     __device__ __forceinline__ void operator()(const Acc& acc, const Unit& u, int wr, int wc, int fr, int fq, const LAS float* tab) const {
;     ...
;                 const size_t row = (size_t)u.pm * BM + ai * HALF + wr * 64 + m * 16 + fr; const size_t off = row * D + col0; float ss = 0.f;
; #pragma unroll
;                 for (int bj = 0; bj < 2; ++bj) { f32x4 b0, b1;
;                     if (base32) { b0 = __builtin_nontemporal_load((const f32x4*)(base32 + off + bj * HALF)); b1 = __builtin_nontemporal_load((const f32x4*)(base32 + off + bj * HALF + 4)); }
.LBB0_1924:
	s_or_b64 exec, exec, s[34:35]
	s_mov_b64 s[0:1], 0xa0
	v_lshl_add_u64 v[42:43], v[220:221], 0, s[0:1]
	v_lshlrev_b64 v[34:35], 10, v[42:43]
	v_lshl_add_u64 v[44:45], v[34:35], 0, v[218:219]
	s_mov_b64 s[34:35], -1
	s_and_b64 vcc, exec, s[8:9]
	v_lshl_add_u64 v[46:47], v[44:45], 2, s[10:11]
	s_cbranch_vccnz .LBB0_1926
	s_waitcnt vmcnt(2)
	s_nop 1
	v_mov_b32_e32 v38, v78
	v_mov_b32_e32 v39, v79
	v_mov_b32_e32 v40, v80
	v_mov_b32_e32 v41, v81
	v_mov_b32_e32 v34, v66
	v_mov_b32_e32 v35, v67
	v_mov_b32_e32 v36, v68
	v_mov_b32_e32 v37, v69
	s_mov_b64 s[100:101], 0xb0000
	v_lshl_add_u64 v[226:227], v[252:253], 0, s[100:101]
	global_load_dwordx4 v[78:81], v[226:227], off offset:16 nt
	global_load_dwordx4 v[66:69], v[226:227], off nt
	s_mov_b64 s[34:35], 0

; __device__ __forceinline__ void st16_wt(void* p, u32x4 v) { asm volatile("global_store_dwordx4 %0, %1, off sc1\n\ts_nop 1" :: "v"(p), "v"(v) : "memory"); }
; __device__ __forceinline__ unsigned cvt_pk_bf16(float lo, float hi) { unsigned r; asm volatile("v_cvt_pk_bf16_f32 %0, %1, %2" : "=v"(r) : "v"(lo), "v"(hi)); return r; }
;     __device__ __forceinline__ void operator()(const Acc& acc, const Unit& u, int wr, int wc, int fr, int fq, const LAS float* tab) const {
;     ...
;                 for (int bj = 0; bj < 2; ++bj) { f32x4 b0, b1;
;                     if (base32) { b0 = __builtin_nontemporal_load((const f32x4*)(base32 + off + bj * HALF)); b1 = __builtin_nontemporal_load((const f32x4*)(base32 + off + bj * HALF + 4)); }
;                     else { const u32x4 b4 = rb[ai][m][bj];
;                         b0 = (f32x4){__uint_as_float(b4.x << 16), __uint_as_float(b4.x & 0xFFFF0000u), __uint_as_float(b4.y << 16), __uint_as_float(b4.y & 0xFFFF0000u)};
;                         b1 = (f32x4){__uint_as_float(b4.z << 16), __uint_as_float(b4.z & 0xFFFF0000u), __uint_as_float(b4.w << 16), __uint_as_float(b4.w & 0xFFFF0000u)}; }
;                     const f32x4 o0 = b0 + acc[ai][bj][m][0], o1 = b1 + acc[ai][bj][m][1];
;                     if (out32) {
;                         if (!dry) { *(f32x4*)(out32 + off + bj * HALF) = o0; *(f32x4*)(out32 + off + bj * HALF + 4) = o1; }
;                         continue; }
;                     ss += ((o0[0] * o0[0] + o0[1] * o0[1]) + (o0[2] * o0[2] + o0[3] * o0[3])) + ((o1[0] * o1[0] + o1[1] * o1[1]) + (o1[2] * o1[2] + o1[3] * o1[3]));
;                     u32x4 w; w.x = cvt_pk_bf16(o0[0], o0[1]); w.y = cvt_pk_bf16(o0[2], o0[3]); w.z = cvt_pk_bf16(o1[0], o1[1]); w.w = cvt_pk_bf16(o1[2], o1[3]);
;                     if (!dry) st16_wt(xb + off + bj * HALF, w); }
.LBB0_1928:
	v_lshl_add_u64 v[44:45], v[44:45], 1, s[14:15]
	v_pk_add_f32 v[36:37], v[32:33], v[36:37]
	v_pk_add_f32 v[48:49], v[30:31], v[34:35]
	v_pk_add_f32 v[34:35], v[28:29], v[40:41]
	v_pk_add_f32 v[38:39], v[26:27], v[38:39]
	v_cvt_pk_bf16_f32 v26, v48, v49
	v_cvt_pk_bf16_f32 v27, v36, v37
	s_and_b64 vcc, exec, s[8:9]
	v_cvt_pk_bf16_f32 v28, v38, v39
	v_cvt_pk_bf16_f32 v29, v34, v35
	s_mov_b64 s[34:35], -1
	global_store_dwordx4 v[44:45], v[26:29], off sc1
	s_nop 1
	s_cbranch_vccnz .LBB0_1930
	s_waitcnt vmcnt(2)
	s_nop 1
	v_mov_b32_e32 v30, v244
	v_mov_b32_e32 v31, v245
	v_mov_b32_e32 v32, v246
	v_mov_b32_e32 v33, v247
	v_mov_b32_e32 v26, v248
	v_mov_b32_e32 v27, v249
	v_mov_b32_e32 v28, v250
	v_mov_b32_e32 v29, v251
	s_mov_b64 s[100:101], 0xb0200
	v_lshl_add_u64 v[226:227], v[252:253], 0, s[100:101]
	global_load_dwordx4 v[244:247], v[226:227], off offset:16 nt
	global_load_dwordx4 v[248:251], v[226:227], off nt
	s_mov_b64 s[34:35], 0

;     __device__ __forceinline__ void operator()(const Acc& acc, const Unit& u, int wr, int wc, int fr, int fq, const LAS float* tab) const {
;     ...
;                 const size_t row = (size_t)u.pm * BM + ai * HALF + wr * 64 + m * 16 + fr; const size_t off = row * D + col0; float ss = 0.f;
; #pragma unroll
;                 for (int bj = 0; bj < 2; ++bj) { f32x4 b0, b1;
;                     if (base32) { b0 = __builtin_nontemporal_load((const f32x4*)(base32 + off + bj * HALF)); b1 = __builtin_nontemporal_load((const f32x4*)(base32 + off + bj * HALF + 4)); }
.LBB0_1934:
	s_or_b64 exec, exec, s[34:35]
	s_mov_b64 s[0:1], 0xb0
	v_lshl_add_u64 v[26:27], v[220:221], 0, s[0:1]
	v_lshlrev_b64 v[18:19], 10, v[26:27]
	v_lshl_add_u64 v[28:29], v[18:19], 0, v[218:219]
	s_mov_b64 s[34:35], -1
	s_and_b64 vcc, exec, s[8:9]
	v_lshl_add_u64 v[30:31], v[28:29], 2, s[10:11]
	s_cbranch_vccnz .LBB0_1936
	s_waitcnt vmcnt(2)
	s_nop 1
	v_mov_b32_e32 v22, v78
	v_mov_b32_e32 v23, v79
	v_mov_b32_e32 v24, v80
	v_mov_b32_e32 v25, v81
	v_mov_b32_e32 v18, v66
	v_mov_b32_e32 v19, v67
	v_mov_b32_e32 v20, v68
	v_mov_b32_e32 v21, v69
	s_mov_b64 s[34:35], 0

; __device__ __forceinline__ void st16_wt(void* p, u32x4 v) { asm volatile("global_store_dwordx4 %0, %1, off sc1\n\ts_nop 1" :: "v"(p), "v"(v) : "memory"); }
; __device__ __forceinline__ unsigned cvt_pk_bf16(float lo, float hi) { unsigned r; asm volatile("v_cvt_pk_bf16_f32 %0, %1, %2" : "=v"(r) : "v"(lo), "v"(hi)); return r; }
;     __device__ __forceinline__ void operator()(const Acc& acc, const Unit& u, int wr, int wc, int fr, int fq, const LAS float* tab) const {
;     ...
;                 for (int bj = 0; bj < 2; ++bj) { f32x4 b0, b1;
;                     if (base32) { b0 = __builtin_nontemporal_load((const f32x4*)(base32 + off + bj * HALF)); b1 = __builtin_nontemporal_load((const f32x4*)(base32 + off + bj * HALF + 4)); }
;                     else { const u32x4 b4 = rb[ai][m][bj];
;                         b0 = (f32x4){__uint_as_float(b4.x << 16), __uint_as_float(b4.x & 0xFFFF0000u), __uint_as_float(b4.y << 16), __uint_as_float(b4.y & 0xFFFF0000u)};
;                         b1 = (f32x4){__uint_as_float(b4.z << 16), __uint_as_float(b4.z & 0xFFFF0000u), __uint_as_float(b4.w << 16), __uint_as_float(b4.w & 0xFFFF0000u)}; }
;                     const f32x4 o0 = b0 + acc[ai][bj][m][0], o1 = b1 + acc[ai][bj][m][1];
;                     if (out32) {
;                         if (!dry) { *(f32x4*)(out32 + off + bj * HALF) = o0; *(f32x4*)(out32 + off + bj * HALF + 4) = o1; }
;                         continue; }
;                     ss += ((o0[0] * o0[0] + o0[1] * o0[1]) + (o0[2] * o0[2] + o0[3] * o0[3])) + ((o1[0] * o1[0] + o1[1] * o1[1]) + (o1[2] * o1[2] + o1[3] * o1[3]));
;                     u32x4 w; w.x = cvt_pk_bf16(o0[0], o0[1]); w.y = cvt_pk_bf16(o0[2], o0[3]); w.z = cvt_pk_bf16(o1[0], o1[1]); w.w = cvt_pk_bf16(o1[2], o1[3]);
;                     if (!dry) st16_wt(xb + off + bj * HALF, w); }
.LBB0_1938:
	v_lshl_add_u64 v[28:29], v[28:29], 1, s[14:15]
	v_pk_add_f32 v[20:21], v[16:17], v[20:21]
	v_pk_add_f32 v[32:33], v[14:15], v[18:19]
	v_pk_add_f32 v[18:19], v[12:13], v[24:25]
	v_pk_add_f32 v[22:23], v[10:11], v[22:23]
	v_cvt_pk_bf16_f32 v10, v32, v33
	v_cvt_pk_bf16_f32 v11, v20, v21
	s_and_b64 vcc, exec, s[8:9]
	v_cvt_pk_bf16_f32 v12, v22, v23
	v_cvt_pk_bf16_f32 v13, v18, v19
	s_mov_b64 s[8:9], -1
	global_store_dwordx4 v[28:29], v[10:13], off sc1
	s_nop 1
	s_cbranch_vccnz .LBB0_1940
	s_waitcnt vmcnt(0)
	s_nop 1
	v_mov_b32_e32 v14, v244
	v_mov_b32_e32 v15, v245
	v_mov_b32_e32 v16, v246
	v_mov_b32_e32 v17, v247
	v_mov_b32_e32 v10, v248
	v_mov_b32_e32 v11, v249
	v_mov_b32_e32 v12, v250
	v_mov_b32_e32 v13, v251
	s_mov_b64 s[8:9], 0
